# G2 and UP fp8 GEMM K-loops: first trip peeled with SrcC=0 instead of 128 v_mov accumulator zeroing per unit (on top of the ATT0 loop edits)
# speedup vs baseline: 1.0032x; 1.0032x over previous
.LBB0_334:
	v_mov_b32_e32 v161, v137
	v_mov_b32_e32 v163, v137
	s_mov_b64 s[44:45], 0
	s_mov_b64 s[10:11], -1
	s_mov_b64 s[42:43], 0
	s_add_u32 s52, s14, s44
	s_addc_u32 s53, s15, s45
	s_add_u32 s46, s52, 0x100
	s_addc_u32 s47, s53, 0
	s_and_b64 s[0:1], s[42:43], exec
	s_cselect_b32 s46, s14, s46
	s_cselect_b32 s47, s15, s47
	s_add_u32 s0, s40, s44
	s_addc_u32 s1, s41, s45
	s_add_u32 s44, s0, 0x100
	s_addc_u32 s45, s1, 0
	ds_read_b128 v[196:199], v170
	ds_read_b128 v[204:207], v170 offset:2048
	ds_read_b128 v[200:203], v171
	ds_read_b128 v[208:211], v171 offset:2048
	s_and_b64 s[0:1], s[42:43], exec
	s_cselect_b32 s51, s37, s45
	s_cselect_b32 s50, s36, s44
	s_add_i32 m0, s58, 0xc000
	s_add_i32 s0, s58, 0xe000
	s_add_u32 s48, s50, 0x1000
	s_addc_u32 s49, s51, 0
	s_add_u32 s44, s50, 0x1080
	s_addc_u32 s45, s51, 0
	v_cndmask_b32_e64 v136, v156, v148, s[42:43]
	s_waitcnt lgkmcnt(0)
	v_cndmask_b32_e64 v149, v160, v152, s[42:43]
	v_lshl_add_u64 v[164:165], s[52:53], 0, v[160:161]
	v_lshl_add_u64 v[164:165], v[164:165], 0, s[26:27]
	ds_read_b128 v[212:215], v129
	ds_read_b128 v[220:223], v129 offset:2048
	ds_read_b128 v[216:219], v133
	ds_read_b128 v[224:227], v133 offset:2048
	ds_read_b128 v[228:231], v129 offset:4096
	ds_read_b128 v[236:239], v129 offset:6144
	ds_read_b128 v[232:235], v133 offset:4096
	ds_read_b128 v[240:243], v133 offset:6144
	global_load_lds_dwordx4 v[164:165], off
	v_lshl_add_u64 v[164:165], s[52:53], 0, v[162:163]
	v_lshl_add_u64 v[164:165], v[164:165], 0, s[26:27]
	s_mov_b32 m0, s0
	s_nop 0
	global_load_lds_dwordx4 v[164:165], off
	s_waitcnt lgkmcnt(8)
	s_barrier
	s_waitcnt lgkmcnt(0)
	v_cndmask_b32_e64 v164, v158, v150, s[42:43]
	s_setprio 1
	s_waitcnt lgkmcnt(0)
	v_mfma_f32_16x16x128_f8f6f4 v[124:127], v[196:203], v[212:219], 0
	v_mfma_f32_16x16x128_f8f6f4 v[120:123], v[204:211], v[212:219], 0
	v_mfma_f32_16x16x128_f8f6f4 v[108:111], v[196:203], v[220:227], 0
	v_mfma_f32_16x16x128_f8f6f4 v[104:107], v[204:211], v[220:227], 0
	v_mfma_f32_16x16x128_f8f6f4 v[92:95], v[196:203], v[228:235], 0
	v_mfma_f32_16x16x128_f8f6f4 v[88:91], v[204:211], v[228:235], 0
	v_mfma_f32_16x16x128_f8f6f4 v[76:79], v[196:203], v[236:243], 0
	v_mfma_f32_16x16x128_f8f6f4 v[72:75], v[204:211], v[236:243], 0
	s_setprio 0
	s_barrier
	ds_read_b128 v[196:199], v170 offset:16384
	ds_read_b128 v[204:207], v170 offset:18432
	ds_read_b128 v[200:203], v171 offset:16384
	ds_read_b128 v[208:211], v171 offset:18432
	s_barrier
	s_waitcnt lgkmcnt(0)
	s_setprio 1
	s_waitcnt lgkmcnt(0)
	v_mfma_f32_16x16x128_f8f6f4 v[116:119], v[196:203], v[212:219], 0
	v_mfma_f32_16x16x128_f8f6f4 v[112:115], v[204:211], v[212:219], 0
	v_mfma_f32_16x16x128_f8f6f4 v[100:103], v[196:203], v[220:227], 0
	v_mfma_f32_16x16x128_f8f6f4 v[96:99], v[204:211], v[220:227], 0
	v_mfma_f32_16x16x128_f8f6f4 v[84:87], v[196:203], v[228:235], 0
	v_mfma_f32_16x16x128_f8f6f4 v[80:83], v[204:211], v[228:235], 0
	v_mfma_f32_16x16x128_f8f6f4 v[68:71], v[196:203], v[236:243], 0
	v_mfma_f32_16x16x128_f8f6f4 v[64:67], v[204:211], v[236:243], 0
	s_setprio 0
	s_barrier
	ds_read_b128 v[196:199], v170
	ds_read_b128 v[204:207], v170 offset:2048
	ds_read_b128 v[200:203], v171
	ds_read_b128 v[208:211], v171 offset:2048
	s_mov_b32 m0, s58
	ds_read_b128 v[212:215], v129 offset:16384
	ds_read_b128 v[220:223], v129 offset:18432
	ds_read_b128 v[216:219], v133 offset:16384
	ds_read_b128 v[224:227], v133 offset:18432
	ds_read_b128 v[228:231], v129 offset:20480
	ds_read_b128 v[236:239], v129 offset:22528
	ds_read_b128 v[232:235], v133 offset:20480
	ds_read_b128 v[240:243], v133 offset:22528
	global_load_lds_dwordx4 v136, s[46:47]
	s_mov_b32 m0, s61
	v_mov_b32_e32 v165, v137
	global_load_lds_dwordx4 v164, s[46:47]
	s_waitcnt lgkmcnt(8)
	s_barrier
	s_waitcnt lgkmcnt(0)
	v_lshl_add_u64 v[168:169], s[46:47], 0, v[136:137]
	v_lshl_add_u64 v[190:191], s[46:47], 0, v[164:165]
	s_setprio 1
	s_waitcnt lgkmcnt(0)
	v_mfma_f32_16x16x128_f8f6f4 v[60:63], v[196:203], v[212:219], 0
	v_mfma_f32_16x16x128_f8f6f4 v[56:59], v[204:211], v[212:219], 0
	v_mfma_f32_16x16x128_f8f6f4 v[44:47], v[196:203], v[220:227], 0
	v_mfma_f32_16x16x128_f8f6f4 v[40:43], v[204:211], v[220:227], 0
	v_mfma_f32_16x16x128_f8f6f4 v[28:31], v[196:203], v[228:235], 0
	v_mfma_f32_16x16x128_f8f6f4 v[24:27], v[204:211], v[228:235], 0
	v_mfma_f32_16x16x128_f8f6f4 v[12:15], v[196:203], v[236:243], 0
	v_mfma_f32_16x16x128_f8f6f4 v[8:11], v[204:211], v[236:243], 0
	s_setprio 0
	s_barrier
	s_mov_b32 m0, s59
	v_lshl_add_u64 v[164:165], s[50:51], 0, v[130:131]
	ds_read_b128 v[196:199], v170 offset:16384
	ds_read_b128 v[204:207], v170 offset:18432
	ds_read_b128 v[200:203], v171 offset:16384
	ds_read_b128 v[208:211], v171 offset:18432
	global_load_lds_dwordx4 v[164:165], off
	v_lshl_add_u64 v[166:167], s[50:51], 0, v[134:135]
	s_mov_b32 m0, s60
	s_nop 0
	global_load_lds_dwordx4 v[166:167], off
	s_waitcnt vmcnt(4)
	s_waitcnt lgkmcnt(0)
	s_barrier
	s_setprio 1
	s_waitcnt lgkmcnt(0)
	v_mfma_f32_16x16x128_f8f6f4 v[52:55], v[196:203], v[212:219], 0
	v_mfma_f32_16x16x128_f8f6f4 v[48:51], v[204:211], v[212:219], 0
	v_mfma_f32_16x16x128_f8f6f4 v[36:39], v[196:203], v[220:227], 0
	v_mfma_f32_16x16x128_f8f6f4 v[32:35], v[204:211], v[220:227], 0
	v_mfma_f32_16x16x128_f8f6f4 v[20:23], v[196:203], v[228:235], 0
	v_mfma_f32_16x16x128_f8f6f4 v[16:19], v[204:211], v[228:235], 0
	v_mfma_f32_16x16x128_f8f6f4 v[4:7], v[196:203], v[236:243], 0
	v_mfma_f32_16x16x128_f8f6f4 v[0:3], v[204:211], v[236:243], 0
	s_setprio 0
	s_barrier
	ds_read_b128 v[196:199], v170 offset:32768
	ds_read_b128 v[204:207], v170 offset:34816
	ds_read_b128 v[200:203], v171 offset:32768
	ds_read_b128 v[208:211], v171 offset:34816
	s_mov_b32 m0, s64
	ds_read_b128 v[212:215], v129 offset:32768
	ds_read_b128 v[220:223], v129 offset:34816
	ds_read_b128 v[216:219], v133 offset:32768
	ds_read_b128 v[224:227], v133 offset:34816
	ds_read_b128 v[228:231], v129 offset:36864
	ds_read_b128 v[236:239], v129 offset:38912
	ds_read_b128 v[232:235], v133 offset:36864
	ds_read_b128 v[240:243], v133 offset:38912
	v_cndmask_b32_e64 v136, v162, v154, s[42:43]
	global_load_lds_dwordx4 v149, s[46:47]
	s_mov_b32 m0, s65
	v_lshl_add_u64 v[192:193], s[48:49], 0, v[130:131]
	global_load_lds_dwordx4 v136, s[46:47]
	s_mov_b32 m0, s62
	s_nop 0
	global_load_lds_dwordx4 v[192:193], off
	v_lshl_add_u64 v[192:193], s[48:49], 0, v[134:135]
	s_mov_b32 m0, s63
	s_nop 0
	global_load_lds_dwordx4 v[192:193], off
	s_waitcnt lgkmcnt(8)
	s_barrier
	s_waitcnt lgkmcnt(0)
	s_setprio 1
	s_waitcnt lgkmcnt(0)
	v_mfma_f32_16x16x128_f8f6f4 v[124:127], v[196:203], v[212:219], v[124:127]
	v_mfma_f32_16x16x128_f8f6f4 v[120:123], v[204:211], v[212:219], v[120:123]
	v_mfma_f32_16x16x128_f8f6f4 v[108:111], v[196:203], v[220:227], v[108:111]
	v_mfma_f32_16x16x128_f8f6f4 v[104:107], v[204:211], v[220:227], v[104:107]
	v_mfma_f32_16x16x128_f8f6f4 v[92:95], v[196:203], v[228:235], v[92:95]
	v_mfma_f32_16x16x128_f8f6f4 v[88:91], v[204:211], v[228:235], v[88:91]
	v_mfma_f32_16x16x128_f8f6f4 v[76:79], v[196:203], v[236:243], v[76:79]
	v_mfma_f32_16x16x128_f8f6f4 v[72:75], v[204:211], v[236:243], v[72:75]
	s_setprio 0
	s_barrier
	ds_read_b128 v[196:199], v170 offset:49152
	ds_read_b128 v[204:207], v170 offset:51200
	ds_read_b128 v[200:203], v171 offset:49152
	ds_read_b128 v[208:211], v171 offset:51200
	s_barrier
	s_waitcnt lgkmcnt(0)
	s_setprio 1
	s_waitcnt lgkmcnt(0)
	v_mfma_f32_16x16x128_f8f6f4 v[116:119], v[196:203], v[212:219], v[116:119]
	v_mfma_f32_16x16x128_f8f6f4 v[112:115], v[204:211], v[212:219], v[112:115]
	v_mfma_f32_16x16x128_f8f6f4 v[100:103], v[196:203], v[220:227], v[100:103]
	v_mfma_f32_16x16x128_f8f6f4 v[96:99], v[204:211], v[220:227], v[96:99]
	v_mfma_f32_16x16x128_f8f6f4 v[84:87], v[196:203], v[228:235], v[84:87]
	v_mfma_f32_16x16x128_f8f6f4 v[80:83], v[204:211], v[228:235], v[80:83]
	v_mfma_f32_16x16x128_f8f6f4 v[68:71], v[196:203], v[236:243], v[68:71]
	v_mfma_f32_16x16x128_f8f6f4 v[64:67], v[204:211], v[236:243], v[64:67]
	s_setprio 0
	s_barrier
	ds_read_b128 v[196:199], v170 offset:32768
	ds_read_b128 v[204:207], v170 offset:34816
	ds_read_b128 v[200:203], v171 offset:32768
	ds_read_b128 v[208:211], v171 offset:34816
	s_mov_b32 m0, s69
	v_lshl_add_u64 v[168:169], v[168:169], 0, s[26:27]
	ds_read_b128 v[212:215], v129 offset:49152
	ds_read_b128 v[220:223], v129 offset:51200
	ds_read_b128 v[216:219], v133 offset:49152
	ds_read_b128 v[224:227], v133 offset:51200
	ds_read_b128 v[228:231], v129 offset:53248
	ds_read_b128 v[236:239], v129 offset:55296
	ds_read_b128 v[232:235], v133 offset:53248
	ds_read_b128 v[240:243], v133 offset:55296
	global_load_lds_dwordx4 v[168:169], off
	v_lshl_add_u64 v[168:169], v[190:191], 0, s[26:27]
	s_mov_b32 m0, s70
	s_nop 0
	global_load_lds_dwordx4 v[168:169], off
	s_waitcnt lgkmcnt(8)
	s_barrier
	s_waitcnt lgkmcnt(0)
	s_setprio 1
	s_waitcnt lgkmcnt(0)
	v_mfma_f32_16x16x128_f8f6f4 v[60:63], v[196:203], v[212:219], v[60:63]
	v_mfma_f32_16x16x128_f8f6f4 v[56:59], v[204:211], v[212:219], v[56:59]
	v_mfma_f32_16x16x128_f8f6f4 v[44:47], v[196:203], v[220:227], v[44:47]
	v_mfma_f32_16x16x128_f8f6f4 v[40:43], v[204:211], v[220:227], v[40:43]
	v_mfma_f32_16x16x128_f8f6f4 v[28:31], v[196:203], v[228:235], v[28:31]
	v_mfma_f32_16x16x128_f8f6f4 v[24:27], v[204:211], v[228:235], v[24:27]
	v_mfma_f32_16x16x128_f8f6f4 v[12:15], v[196:203], v[236:243], v[12:15]
	v_mfma_f32_16x16x128_f8f6f4 v[8:11], v[204:211], v[236:243], v[8:11]
	s_setprio 0
	s_barrier
	s_mov_b32 m0, s67
	v_lshl_add_u64 v[164:165], v[164:165], 0, s[26:27]
	ds_read_b128 v[196:199], v170 offset:49152
	ds_read_b128 v[204:207], v170 offset:51200
	ds_read_b128 v[200:203], v171 offset:49152
	ds_read_b128 v[208:211], v171 offset:51200
	global_load_lds_dwordx4 v[164:165], off
	v_lshl_add_u64 v[164:165], v[166:167], 0, s[26:27]
	s_mov_b32 m0, s68
	s_nop 0
	global_load_lds_dwordx4 v[164:165], off
	s_waitcnt vmcnt(4)
	s_waitcnt lgkmcnt(0)
	s_barrier
	s_setprio 1
	s_waitcnt lgkmcnt(0)
	v_mfma_f32_16x16x128_f8f6f4 v[52:55], v[196:203], v[212:219], v[52:55]
	v_mfma_f32_16x16x128_f8f6f4 v[48:51], v[204:211], v[212:219], v[48:51]
	v_mfma_f32_16x16x128_f8f6f4 v[36:39], v[196:203], v[220:227], v[36:39]
	v_mfma_f32_16x16x128_f8f6f4 v[32:35], v[204:211], v[220:227], v[32:35]
	v_mfma_f32_16x16x128_f8f6f4 v[20:23], v[196:203], v[228:235], v[20:23]
	v_mfma_f32_16x16x128_f8f6f4 v[16:19], v[204:211], v[228:235], v[16:19]
	v_mfma_f32_16x16x128_f8f6f4 v[4:7], v[196:203], v[236:243], v[4:7]
	v_mfma_f32_16x16x128_f8f6f4 v[0:3], v[204:211], v[236:243], v[0:3]
	s_setprio 0
	s_barrier
	s_mov_b32 m0, s71
	v_lshl_add_u64 v[164:165], s[44:45], 0, v[130:131]
	global_load_lds_dwordx4 v[164:165], off
	v_lshl_add_u64 v[164:165], s[44:45], 0, v[134:135]
	s_mov_b32 m0, s72
	s_andn2_b64 vcc, exec, s[10:11]
	global_load_lds_dwordx4 v[164:165], off
	s_mov_b64 s[42:43], -1
	s_mov_b64 s[10:11], 0
	s_mov_b64 s[44:45], 0x100
	s_cbranch_vccz .LBB0_335
	s_branch .Lpeel_after_335

.Lpeel_after_335:
	s_and_b64 vcc, exec, s[28:29]
	s_cbranch_vccz .LBB0_338
	s_barrier

.LBB0_1060:
	v_mov_b32_e32 v137, v133
	v_mov_b32_e32 v139, v133
	s_mov_b64 s[44:45], 0
	s_mov_b64 s[40:41], -1
	s_mov_b64 s[42:43], 0
	s_add_u32 s52, s12, s44
	s_addc_u32 s53, s13, s45
	s_add_u32 s29, s52, 0x100
	s_addc_u32 s48, s53, 0
	s_and_b64 s[46:47], s[42:43], exec
	s_cselect_b32 s46, s12, s29
	s_cselect_b32 s47, s13, s48
	s_add_u32 s29, s38, s44
	s_addc_u32 s44, s39, s45
	s_add_u32 s29, s29, 0x100
	s_addc_u32 s48, s44, 0
	ds_read_b128 v[162:165], v147
	ds_read_b128 v[170:173], v147 offset:2048
	ds_read_b128 v[166:169], v148
	ds_read_b128 v[174:177], v148 offset:2048
	s_and_b64 s[44:45], s[42:43], exec
	s_cselect_b32 s51, s35, s48
	s_cselect_b32 s50, s34, s29
	s_add_i32 m0, s0, 0xc000
	s_add_i32 s29, s0, 0xe000
	s_add_u32 s48, s50, 0x1000
	s_addc_u32 s49, s51, 0
	s_add_u32 s44, s50, 0x1080
	s_addc_u32 s45, s51, 0
	v_cndmask_b32_e64 v132, v135, v157, s[42:43]
	v_cndmask_b32_e64 v161, v136, v159, s[42:43]
	v_lshl_add_u64 v[140:141], s[52:53], 0, v[136:137]
	v_lshl_add_u64 v[140:141], v[140:141], 0, s[20:21]
	ds_read_b128 v[178:181], v145
	ds_read_b128 v[186:189], v145 offset:2048
	ds_read_b128 v[182:185], v146
	ds_read_b128 v[190:193], v146 offset:2048
	ds_read_b128 v[196:199], v145 offset:4096
	ds_read_b128 v[204:207], v145 offset:6144
	ds_read_b128 v[200:203], v146 offset:4096
	ds_read_b128 v[208:211], v146 offset:6144
	global_load_lds_dwordx4 v[140:141], off
	v_lshl_add_u64 v[140:141], s[52:53], 0, v[138:139]
	v_lshl_add_u64 v[140:141], v[140:141], 0, s[20:21]
	s_mov_b32 m0, s29
	s_nop 0
	global_load_lds_dwordx4 v[140:141], off
	s_waitcnt lgkmcnt(8)
	s_barrier
	s_waitcnt lgkmcnt(0)
	v_cndmask_b32_e64 v140, v134, v158, s[42:43]
	s_setprio 1
	s_waitcnt lgkmcnt(0)
	v_mfma_f32_16x16x128_f8f6f4 v[124:127], v[162:169], v[178:185], 0
	v_mfma_f32_16x16x128_f8f6f4 v[120:123], v[170:177], v[178:185], 0
	v_mfma_f32_16x16x128_f8f6f4 v[108:111], v[162:169], v[186:193], 0
	v_mfma_f32_16x16x128_f8f6f4 v[104:107], v[170:177], v[186:193], 0
	v_mfma_f32_16x16x128_f8f6f4 v[92:95], v[162:169], v[196:203], 0
	v_mfma_f32_16x16x128_f8f6f4 v[88:91], v[170:177], v[196:203], 0
	v_mfma_f32_16x16x128_f8f6f4 v[76:79], v[162:169], v[204:211], 0
	v_mfma_f32_16x16x128_f8f6f4 v[72:75], v[170:177], v[204:211], 0
	s_setprio 0
	s_barrier
	ds_read_b128 v[162:165], v147 offset:16384
	ds_read_b128 v[170:173], v147 offset:18432
	ds_read_b128 v[166:169], v148 offset:16384
	ds_read_b128 v[174:177], v148 offset:18432
	s_barrier
	s_waitcnt lgkmcnt(0)
	s_setprio 1
	s_waitcnt lgkmcnt(0)
	v_mfma_f32_16x16x128_f8f6f4 v[116:119], v[162:169], v[178:185], 0
	v_mfma_f32_16x16x128_f8f6f4 v[112:115], v[170:177], v[178:185], 0
	v_mfma_f32_16x16x128_f8f6f4 v[100:103], v[162:169], v[186:193], 0
	v_mfma_f32_16x16x128_f8f6f4 v[96:99], v[170:177], v[186:193], 0
	v_mfma_f32_16x16x128_f8f6f4 v[84:87], v[162:169], v[196:203], 0
	v_mfma_f32_16x16x128_f8f6f4 v[80:83], v[170:177], v[196:203], 0
	v_mfma_f32_16x16x128_f8f6f4 v[68:71], v[162:169], v[204:211], 0
	v_mfma_f32_16x16x128_f8f6f4 v[64:67], v[170:177], v[204:211], 0
	s_setprio 0
	s_barrier
	ds_read_b128 v[162:165], v147
	ds_read_b128 v[170:173], v147 offset:2048
	ds_read_b128 v[166:169], v148
	ds_read_b128 v[174:177], v148 offset:2048
	s_mov_b32 m0, s0
	ds_read_b128 v[178:181], v145 offset:16384
	ds_read_b128 v[186:189], v145 offset:18432
	ds_read_b128 v[182:185], v146 offset:16384
	ds_read_b128 v[190:193], v146 offset:18432
	ds_read_b128 v[196:199], v145 offset:20480
	ds_read_b128 v[204:207], v145 offset:22528
	ds_read_b128 v[200:203], v146 offset:20480
	ds_read_b128 v[208:211], v146 offset:22528
	global_load_lds_dwordx4 v132, s[46:47]
	s_mov_b32 m0, s56
	v_mov_b32_e32 v141, v133
	global_load_lds_dwordx4 v140, s[46:47]
	s_waitcnt lgkmcnt(8)
	s_barrier
	s_waitcnt lgkmcnt(0)
	v_lshl_add_u64 v[212:213], s[46:47], 0, v[132:133]
	v_lshl_add_u64 v[214:215], s[46:47], 0, v[140:141]
	s_setprio 1
	s_waitcnt lgkmcnt(0)
	v_mfma_f32_16x16x128_f8f6f4 v[60:63], v[162:169], v[178:185], 0
	v_mfma_f32_16x16x128_f8f6f4 v[56:59], v[170:177], v[178:185], 0
	v_mfma_f32_16x16x128_f8f6f4 v[44:47], v[162:169], v[186:193], 0
	v_mfma_f32_16x16x128_f8f6f4 v[40:43], v[170:177], v[186:193], 0
	v_mfma_f32_16x16x128_f8f6f4 v[28:31], v[162:169], v[196:203], 0
	v_mfma_f32_16x16x128_f8f6f4 v[24:27], v[170:177], v[196:203], 0
	v_mfma_f32_16x16x128_f8f6f4 v[12:15], v[162:169], v[204:211], 0
	v_mfma_f32_16x16x128_f8f6f4 v[8:11], v[170:177], v[204:211], 0
	s_setprio 0
	s_barrier
	s_mov_b32 m0, s1
	v_lshl_add_u64 v[140:141], s[50:51], 0, v[128:129]
	ds_read_b128 v[162:165], v147 offset:16384
	ds_read_b128 v[170:173], v147 offset:18432
	ds_read_b128 v[166:169], v148 offset:16384
	ds_read_b128 v[174:177], v148 offset:18432
	global_load_lds_dwordx4 v[140:141], off
	v_lshl_add_u64 v[142:143], s[50:51], 0, v[130:131]
	s_mov_b32 m0, s37
	s_nop 0
	global_load_lds_dwordx4 v[142:143], off
	s_waitcnt vmcnt(4)
	s_waitcnt lgkmcnt(0)
	s_barrier
	s_setprio 1
	s_waitcnt lgkmcnt(0)
	v_mfma_f32_16x16x128_f8f6f4 v[52:55], v[162:169], v[178:185], 0
	v_mfma_f32_16x16x128_f8f6f4 v[48:51], v[170:177], v[178:185], 0
	v_mfma_f32_16x16x128_f8f6f4 v[36:39], v[162:169], v[186:193], 0
	v_mfma_f32_16x16x128_f8f6f4 v[32:35], v[170:177], v[186:193], 0
	v_mfma_f32_16x16x128_f8f6f4 v[20:23], v[162:169], v[196:203], 0
	v_mfma_f32_16x16x128_f8f6f4 v[16:19], v[170:177], v[196:203], 0
	v_mfma_f32_16x16x128_f8f6f4 v[4:7], v[162:169], v[204:211], 0
	v_mfma_f32_16x16x128_f8f6f4 v[0:3], v[170:177], v[204:211], 0
	s_setprio 0
	s_barrier
	ds_read_b128 v[162:165], v147 offset:32768
	ds_read_b128 v[170:173], v147 offset:34816
	ds_read_b128 v[166:169], v148 offset:32768
	ds_read_b128 v[174:177], v148 offset:34816
	s_mov_b32 m0, s63
	ds_read_b128 v[178:181], v145 offset:32768
	ds_read_b128 v[186:189], v145 offset:34816
	ds_read_b128 v[182:185], v146 offset:32768
	ds_read_b128 v[190:193], v146 offset:34816
	ds_read_b128 v[196:199], v145 offset:36864
	ds_read_b128 v[204:207], v145 offset:38912
	ds_read_b128 v[200:203], v146 offset:36864
	ds_read_b128 v[208:211], v146 offset:38912
	v_cndmask_b32_e64 v132, v138, v160, s[42:43]
	global_load_lds_dwordx4 v161, s[46:47]
	s_mov_b32 m0, s64
	v_lshl_add_u64 v[216:217], s[48:49], 0, v[128:129]
	global_load_lds_dwordx4 v132, s[46:47]
	s_mov_b32 m0, s57
	s_nop 0
	global_load_lds_dwordx4 v[216:217], off
	v_lshl_add_u64 v[216:217], s[48:49], 0, v[130:131]
	s_mov_b32 m0, s62
	s_nop 0
	global_load_lds_dwordx4 v[216:217], off
	s_waitcnt lgkmcnt(8)
	s_barrier
	s_waitcnt lgkmcnt(0)
	s_setprio 1
	s_waitcnt lgkmcnt(0)
	v_mfma_f32_16x16x128_f8f6f4 v[124:127], v[162:169], v[178:185], v[124:127]
	v_mfma_f32_16x16x128_f8f6f4 v[120:123], v[170:177], v[178:185], v[120:123]
	v_mfma_f32_16x16x128_f8f6f4 v[108:111], v[162:169], v[186:193], v[108:111]
	v_mfma_f32_16x16x128_f8f6f4 v[104:107], v[170:177], v[186:193], v[104:107]
	v_mfma_f32_16x16x128_f8f6f4 v[92:95], v[162:169], v[196:203], v[92:95]
	v_mfma_f32_16x16x128_f8f6f4 v[88:91], v[170:177], v[196:203], v[88:91]
	v_mfma_f32_16x16x128_f8f6f4 v[76:79], v[162:169], v[204:211], v[76:79]
	v_mfma_f32_16x16x128_f8f6f4 v[72:75], v[170:177], v[204:211], v[72:75]
	s_setprio 0
	s_barrier
	ds_read_b128 v[162:165], v147 offset:49152
	ds_read_b128 v[170:173], v147 offset:51200
	ds_read_b128 v[166:169], v148 offset:49152
	ds_read_b128 v[174:177], v148 offset:51200
	s_barrier
	s_waitcnt lgkmcnt(0)
	s_setprio 1
	s_waitcnt lgkmcnt(0)
	v_mfma_f32_16x16x128_f8f6f4 v[116:119], v[162:169], v[178:185], v[116:119]
	v_mfma_f32_16x16x128_f8f6f4 v[112:115], v[170:177], v[178:185], v[112:115]
	v_mfma_f32_16x16x128_f8f6f4 v[100:103], v[162:169], v[186:193], v[100:103]
	v_mfma_f32_16x16x128_f8f6f4 v[96:99], v[170:177], v[186:193], v[96:99]
	v_mfma_f32_16x16x128_f8f6f4 v[84:87], v[162:169], v[196:203], v[84:87]
	v_mfma_f32_16x16x128_f8f6f4 v[80:83], v[170:177], v[196:203], v[80:83]
	v_mfma_f32_16x16x128_f8f6f4 v[68:71], v[162:169], v[204:211], v[68:71]
	v_mfma_f32_16x16x128_f8f6f4 v[64:67], v[170:177], v[204:211], v[64:67]
	s_setprio 0
	s_barrier
	ds_read_b128 v[162:165], v147 offset:32768
	ds_read_b128 v[170:173], v147 offset:34816
	ds_read_b128 v[166:169], v148 offset:32768
	ds_read_b128 v[174:177], v148 offset:34816
	s_mov_b32 m0, s67
	v_lshl_add_u64 v[212:213], v[212:213], 0, s[20:21]
	ds_read_b128 v[178:181], v145 offset:49152
	ds_read_b128 v[186:189], v145 offset:51200
	ds_read_b128 v[182:185], v146 offset:49152
	ds_read_b128 v[190:193], v146 offset:51200
	ds_read_b128 v[196:199], v145 offset:53248
	ds_read_b128 v[204:207], v145 offset:55296
	ds_read_b128 v[200:203], v146 offset:53248
	ds_read_b128 v[208:211], v146 offset:55296
	global_load_lds_dwordx4 v[212:213], off
	v_lshl_add_u64 v[212:213], v[214:215], 0, s[20:21]
	s_mov_b32 m0, s68
	s_nop 0
	global_load_lds_dwordx4 v[212:213], off
	s_waitcnt lgkmcnt(8)
	s_barrier
	s_waitcnt lgkmcnt(0)
	s_setprio 1
	s_waitcnt lgkmcnt(0)
	v_mfma_f32_16x16x128_f8f6f4 v[60:63], v[162:169], v[178:185], v[60:63]
	v_mfma_f32_16x16x128_f8f6f4 v[56:59], v[170:177], v[178:185], v[56:59]
	v_mfma_f32_16x16x128_f8f6f4 v[44:47], v[162:169], v[186:193], v[44:47]
	v_mfma_f32_16x16x128_f8f6f4 v[40:43], v[170:177], v[186:193], v[40:43]
	v_mfma_f32_16x16x128_f8f6f4 v[28:31], v[162:169], v[196:203], v[28:31]
	v_mfma_f32_16x16x128_f8f6f4 v[24:27], v[170:177], v[196:203], v[24:27]
	v_mfma_f32_16x16x128_f8f6f4 v[12:15], v[162:169], v[204:211], v[12:15]
	v_mfma_f32_16x16x128_f8f6f4 v[8:11], v[170:177], v[204:211], v[8:11]
	s_setprio 0
	s_barrier
	s_mov_b32 m0, s65
	v_lshl_add_u64 v[140:141], v[140:141], 0, s[20:21]
	ds_read_b128 v[162:165], v147 offset:49152
	ds_read_b128 v[170:173], v147 offset:51200
	ds_read_b128 v[166:169], v148 offset:49152
	ds_read_b128 v[174:177], v148 offset:51200
	global_load_lds_dwordx4 v[140:141], off
	v_lshl_add_u64 v[140:141], v[142:143], 0, s[20:21]
	s_mov_b32 m0, s66
	s_nop 0
	global_load_lds_dwordx4 v[140:141], off
	s_waitcnt vmcnt(4)
	s_waitcnt lgkmcnt(0)
	s_barrier
	s_setprio 1
	s_waitcnt lgkmcnt(0)
	v_mfma_f32_16x16x128_f8f6f4 v[52:55], v[162:169], v[178:185], v[52:55]
	v_mfma_f32_16x16x128_f8f6f4 v[48:51], v[170:177], v[178:185], v[48:51]
	v_mfma_f32_16x16x128_f8f6f4 v[36:39], v[162:169], v[186:193], v[36:39]
	v_mfma_f32_16x16x128_f8f6f4 v[32:35], v[170:177], v[186:193], v[32:35]
	v_mfma_f32_16x16x128_f8f6f4 v[20:23], v[162:169], v[196:203], v[20:23]
	v_mfma_f32_16x16x128_f8f6f4 v[16:19], v[170:177], v[196:203], v[16:19]
	v_mfma_f32_16x16x128_f8f6f4 v[4:7], v[162:169], v[204:211], v[4:7]
	v_mfma_f32_16x16x128_f8f6f4 v[0:3], v[170:177], v[204:211], v[0:3]
	s_setprio 0
	s_barrier
	s_mov_b32 m0, s69
	v_lshl_add_u64 v[140:141], s[44:45], 0, v[128:129]
	global_load_lds_dwordx4 v[140:141], off
	v_lshl_add_u64 v[140:141], s[44:45], 0, v[130:131]
	s_mov_b32 m0, s70
	s_andn2_b64 vcc, exec, s[40:41]
	global_load_lds_dwordx4 v[140:141], off
	s_mov_b64 s[42:43], -1
	s_mov_b64 s[40:41], 0
	s_mov_b64 s[44:45], 0x100
	s_cbranch_vccz .LBB0_1061
	s_branch .Lpeel_after_1061

.Lpeel_after_1061:
	s_and_b64 vcc, exec, s[24:25]
	s_cbranch_vccz .LBB0_1064
	s_barrier

.LBB0_1080:
	v_mov_b32_e32 v137, v133
	v_mov_b32_e32 v139, v133
	s_mov_b64 s[34:35], 0
	s_mov_b64 s[28:29], -1
	s_mov_b64 s[30:31], 0
	s_add_u32 s42, s10, s34
	s_addc_u32 s43, s11, s35
	s_add_u32 s38, s42, 0x100
	s_addc_u32 s39, s43, 0
	s_and_b64 s[36:37], s[30:31], exec
	s_cselect_b32 s36, s10, s38
	s_cselect_b32 s37, s11, s39
	s_add_u32 s34, s26, s34
	s_addc_u32 s35, s27, s35
	s_add_u32 s38, s34, 0x100
	s_addc_u32 s39, s35, 0
	ds_read_b128 v[160:163], v147
	ds_read_b128 v[168:171], v147 offset:2048
	ds_read_b128 v[164:167], v148
	ds_read_b128 v[172:175], v148 offset:2048
	s_and_b64 s[34:35], s[30:31], exec
	s_cselect_b32 s41, s25, s39
	s_cselect_b32 s40, s24, s38
	s_add_i32 m0, s1, 0xc000
	s_add_i32 s64, s1, 0xe000
	s_add_u32 s38, s40, 0x1000
	s_addc_u32 s39, s41, 0
	s_add_u32 s34, s40, 0x1080
	s_addc_u32 s35, s41, 0
	v_cndmask_b32_e64 v132, v135, v155, s[30:31]
	v_cndmask_b32_e64 v159, v136, v157, s[30:31]
	v_lshl_add_u64 v[140:141], s[42:43], 0, v[136:137]
	v_lshl_add_u64 v[140:141], v[140:141], 0, s[16:17]
	ds_read_b128 v[176:179], v145
	ds_read_b128 v[184:187], v145 offset:2048
	ds_read_b128 v[180:183], v146
	ds_read_b128 v[188:191], v146 offset:2048
	ds_read_b128 v[196:199], v145 offset:4096
	ds_read_b128 v[204:207], v145 offset:6144
	ds_read_b128 v[200:203], v146 offset:4096
	ds_read_b128 v[208:211], v146 offset:6144
	global_load_lds_dwordx4 v[140:141], off
	v_lshl_add_u64 v[140:141], s[42:43], 0, v[138:139]
	v_lshl_add_u64 v[140:141], v[140:141], 0, s[16:17]
	s_mov_b32 m0, s64
	s_nop 0
	global_load_lds_dwordx4 v[140:141], off
	s_waitcnt lgkmcnt(8)
	s_barrier
	s_waitcnt lgkmcnt(0)
	v_cndmask_b32_e64 v140, v134, v156, s[30:31]
	s_setprio 1
	s_waitcnt lgkmcnt(0)
	v_mfma_f32_16x16x128_f8f6f4 v[124:127], v[160:167], v[176:183], 0
	v_mfma_f32_16x16x128_f8f6f4 v[120:123], v[168:175], v[176:183], 0
	v_mfma_f32_16x16x128_f8f6f4 v[108:111], v[160:167], v[184:191], 0
	v_mfma_f32_16x16x128_f8f6f4 v[104:107], v[168:175], v[184:191], 0
	v_mfma_f32_16x16x128_f8f6f4 v[92:95], v[160:167], v[196:203], 0
	v_mfma_f32_16x16x128_f8f6f4 v[88:91], v[168:175], v[196:203], 0
	v_mfma_f32_16x16x128_f8f6f4 v[76:79], v[160:167], v[204:211], 0
	v_mfma_f32_16x16x128_f8f6f4 v[72:75], v[168:175], v[204:211], 0
	s_setprio 0
	s_barrier
	ds_read_b128 v[160:163], v147 offset:16384
	ds_read_b128 v[168:171], v147 offset:18432
	ds_read_b128 v[164:167], v148 offset:16384
	ds_read_b128 v[172:175], v148 offset:18432
	s_barrier
	s_waitcnt lgkmcnt(0)
	s_setprio 1
	s_waitcnt lgkmcnt(0)
	v_mfma_f32_16x16x128_f8f6f4 v[116:119], v[160:167], v[176:183], 0
	v_mfma_f32_16x16x128_f8f6f4 v[112:115], v[168:175], v[176:183], 0
	v_mfma_f32_16x16x128_f8f6f4 v[100:103], v[160:167], v[184:191], 0
	v_mfma_f32_16x16x128_f8f6f4 v[96:99], v[168:175], v[184:191], 0
	v_mfma_f32_16x16x128_f8f6f4 v[84:87], v[160:167], v[196:203], 0
	v_mfma_f32_16x16x128_f8f6f4 v[80:83], v[168:175], v[196:203], 0
	v_mfma_f32_16x16x128_f8f6f4 v[68:71], v[160:167], v[204:211], 0
	v_mfma_f32_16x16x128_f8f6f4 v[64:67], v[168:175], v[204:211], 0
	s_setprio 0
	s_barrier
	ds_read_b128 v[160:163], v147
	ds_read_b128 v[168:171], v147 offset:2048
	ds_read_b128 v[164:167], v148
	ds_read_b128 v[172:175], v148 offset:2048
	s_mov_b32 m0, s1
	ds_read_b128 v[176:179], v145 offset:16384
	ds_read_b128 v[184:187], v145 offset:18432
	ds_read_b128 v[180:183], v146 offset:16384
	ds_read_b128 v[188:191], v146 offset:18432
	ds_read_b128 v[196:199], v145 offset:20480
	ds_read_b128 v[204:207], v145 offset:22528
	ds_read_b128 v[200:203], v146 offset:20480
	ds_read_b128 v[208:211], v146 offset:22528
	global_load_lds_dwordx4 v132, s[36:37]
	s_mov_b32 m0, s48
	v_mov_b32_e32 v141, v133
	global_load_lds_dwordx4 v140, s[36:37]
	s_waitcnt lgkmcnt(8)
	s_barrier
	s_waitcnt lgkmcnt(0)
	v_lshl_add_u64 v[192:193], s[36:37], 0, v[132:133]
	v_lshl_add_u64 v[212:213], s[36:37], 0, v[140:141]
	s_setprio 1
	s_waitcnt lgkmcnt(0)
	v_mfma_f32_16x16x128_f8f6f4 v[60:63], v[160:167], v[176:183], 0
	v_mfma_f32_16x16x128_f8f6f4 v[56:59], v[168:175], v[176:183], 0
	v_mfma_f32_16x16x128_f8f6f4 v[44:47], v[160:167], v[184:191], 0
	v_mfma_f32_16x16x128_f8f6f4 v[40:43], v[168:175], v[184:191], 0
	v_mfma_f32_16x16x128_f8f6f4 v[28:31], v[160:167], v[196:203], 0
	v_mfma_f32_16x16x128_f8f6f4 v[24:27], v[168:175], v[196:203], 0
	v_mfma_f32_16x16x128_f8f6f4 v[12:15], v[160:167], v[204:211], 0
	v_mfma_f32_16x16x128_f8f6f4 v[8:11], v[168:175], v[204:211], 0
	s_setprio 0
	s_barrier
	s_mov_b32 m0, s46
	v_lshl_add_u64 v[140:141], s[40:41], 0, v[130:131]
	ds_read_b128 v[160:163], v147 offset:16384
	ds_read_b128 v[168:171], v147 offset:18432
	ds_read_b128 v[164:167], v148 offset:16384
	ds_read_b128 v[172:175], v148 offset:18432
	global_load_lds_dwordx4 v[140:141], off
	v_lshl_add_u64 v[142:143], s[40:41], 0, v[128:129]
	s_mov_b32 m0, s47
	s_nop 0
	global_load_lds_dwordx4 v[142:143], off
	s_waitcnt vmcnt(4)
	s_waitcnt lgkmcnt(0)
	s_barrier
	s_setprio 1
	s_waitcnt lgkmcnt(0)
	v_mfma_f32_16x16x128_f8f6f4 v[52:55], v[160:167], v[176:183], 0
	v_mfma_f32_16x16x128_f8f6f4 v[48:51], v[168:175], v[176:183], 0
	v_mfma_f32_16x16x128_f8f6f4 v[36:39], v[160:167], v[184:191], 0
	v_mfma_f32_16x16x128_f8f6f4 v[32:35], v[168:175], v[184:191], 0
	v_mfma_f32_16x16x128_f8f6f4 v[20:23], v[160:167], v[196:203], 0
	v_mfma_f32_16x16x128_f8f6f4 v[16:19], v[168:175], v[196:203], 0
	v_mfma_f32_16x16x128_f8f6f4 v[4:7], v[160:167], v[204:211], 0
	v_mfma_f32_16x16x128_f8f6f4 v[0:3], v[168:175], v[204:211], 0
	s_setprio 0
	s_barrier
	ds_read_b128 v[160:163], v147 offset:32768
	ds_read_b128 v[168:171], v147 offset:34816
	ds_read_b128 v[164:167], v148 offset:32768
	ds_read_b128 v[172:175], v148 offset:34816
	s_mov_b32 m0, s51
	ds_read_b128 v[176:179], v145 offset:32768
	ds_read_b128 v[184:187], v145 offset:34816
	ds_read_b128 v[180:183], v146 offset:32768
	ds_read_b128 v[188:191], v146 offset:34816
	ds_read_b128 v[196:199], v145 offset:36864
	ds_read_b128 v[204:207], v145 offset:38912
	ds_read_b128 v[200:203], v146 offset:36864
	ds_read_b128 v[208:211], v146 offset:38912
	v_cndmask_b32_e64 v132, v138, v158, s[30:31]
	global_load_lds_dwordx4 v159, s[36:37]
	s_mov_b32 m0, s52
	v_lshl_add_u64 v[214:215], s[38:39], 0, v[130:131]
	global_load_lds_dwordx4 v132, s[36:37]
	s_mov_b32 m0, s49
	s_nop 0
	global_load_lds_dwordx4 v[214:215], off
	v_lshl_add_u64 v[214:215], s[38:39], 0, v[128:129]
	s_mov_b32 m0, s50
	s_nop 0
	global_load_lds_dwordx4 v[214:215], off
	s_waitcnt lgkmcnt(8)
	s_barrier
	s_waitcnt lgkmcnt(0)
	s_setprio 1
	s_waitcnt lgkmcnt(0)
	v_mfma_f32_16x16x128_f8f6f4 v[124:127], v[160:167], v[176:183], v[124:127]
	v_mfma_f32_16x16x128_f8f6f4 v[120:123], v[168:175], v[176:183], v[120:123]
	v_mfma_f32_16x16x128_f8f6f4 v[108:111], v[160:167], v[184:191], v[108:111]
	v_mfma_f32_16x16x128_f8f6f4 v[104:107], v[168:175], v[184:191], v[104:107]
	v_mfma_f32_16x16x128_f8f6f4 v[92:95], v[160:167], v[196:203], v[92:95]
	v_mfma_f32_16x16x128_f8f6f4 v[88:91], v[168:175], v[196:203], v[88:91]
	v_mfma_f32_16x16x128_f8f6f4 v[76:79], v[160:167], v[204:211], v[76:79]
	v_mfma_f32_16x16x128_f8f6f4 v[72:75], v[168:175], v[204:211], v[72:75]
	s_setprio 0
	s_barrier
	ds_read_b128 v[160:163], v147 offset:49152
	ds_read_b128 v[168:171], v147 offset:51200
	ds_read_b128 v[164:167], v148 offset:49152
	ds_read_b128 v[172:175], v148 offset:51200
	s_barrier
	s_waitcnt lgkmcnt(0)
	s_setprio 1
	s_waitcnt lgkmcnt(0)
	v_mfma_f32_16x16x128_f8f6f4 v[116:119], v[160:167], v[176:183], v[116:119]
	v_mfma_f32_16x16x128_f8f6f4 v[112:115], v[168:175], v[176:183], v[112:115]
	v_mfma_f32_16x16x128_f8f6f4 v[100:103], v[160:167], v[184:191], v[100:103]
	v_mfma_f32_16x16x128_f8f6f4 v[96:99], v[168:175], v[184:191], v[96:99]
	v_mfma_f32_16x16x128_f8f6f4 v[84:87], v[160:167], v[196:203], v[84:87]
	v_mfma_f32_16x16x128_f8f6f4 v[80:83], v[168:175], v[196:203], v[80:83]
	v_mfma_f32_16x16x128_f8f6f4 v[68:71], v[160:167], v[204:211], v[68:71]
	v_mfma_f32_16x16x128_f8f6f4 v[64:67], v[168:175], v[204:211], v[64:67]
	s_setprio 0
	s_barrier
	ds_read_b128 v[160:163], v147 offset:32768
	ds_read_b128 v[168:171], v147 offset:34816
	ds_read_b128 v[164:167], v148 offset:32768
	ds_read_b128 v[172:175], v148 offset:34816
	s_mov_b32 m0, s56
	v_lshl_add_u64 v[192:193], v[192:193], 0, s[16:17]
	ds_read_b128 v[176:179], v145 offset:49152
	ds_read_b128 v[184:187], v145 offset:51200
	ds_read_b128 v[180:183], v146 offset:49152
	ds_read_b128 v[188:191], v146 offset:51200
	ds_read_b128 v[196:199], v145 offset:53248
	ds_read_b128 v[204:207], v145 offset:55296
	ds_read_b128 v[200:203], v146 offset:53248
	ds_read_b128 v[208:211], v146 offset:55296
	global_load_lds_dwordx4 v[192:193], off
	v_lshl_add_u64 v[192:193], v[212:213], 0, s[16:17]
	s_mov_b32 m0, s57
	s_nop 0
	global_load_lds_dwordx4 v[192:193], off
	s_waitcnt lgkmcnt(8)
	s_barrier
	s_waitcnt lgkmcnt(0)
	s_setprio 1
	s_waitcnt lgkmcnt(0)
	v_mfma_f32_16x16x128_f8f6f4 v[60:63], v[160:167], v[176:183], v[60:63]
	v_mfma_f32_16x16x128_f8f6f4 v[56:59], v[168:175], v[176:183], v[56:59]
	v_mfma_f32_16x16x128_f8f6f4 v[44:47], v[160:167], v[184:191], v[44:47]
	v_mfma_f32_16x16x128_f8f6f4 v[40:43], v[168:175], v[184:191], v[40:43]
	v_mfma_f32_16x16x128_f8f6f4 v[28:31], v[160:167], v[196:203], v[28:31]
	v_mfma_f32_16x16x128_f8f6f4 v[24:27], v[168:175], v[196:203], v[24:27]
	v_mfma_f32_16x16x128_f8f6f4 v[12:15], v[160:167], v[204:211], v[12:15]
	v_mfma_f32_16x16x128_f8f6f4 v[8:11], v[168:175], v[204:211], v[8:11]
	s_setprio 0
	s_barrier
	s_mov_b32 m0, s54
	v_lshl_add_u64 v[140:141], v[140:141], 0, s[16:17]
	ds_read_b128 v[160:163], v147 offset:49152
	ds_read_b128 v[168:171], v147 offset:51200
	ds_read_b128 v[164:167], v148 offset:49152
	ds_read_b128 v[172:175], v148 offset:51200
	global_load_lds_dwordx4 v[140:141], off
	v_lshl_add_u64 v[140:141], v[142:143], 0, s[16:17]
	s_mov_b32 m0, s55
	s_nop 0
	global_load_lds_dwordx4 v[140:141], off
	s_waitcnt vmcnt(4)
	s_waitcnt lgkmcnt(0)
	s_barrier
	s_setprio 1
	s_waitcnt lgkmcnt(0)
	v_mfma_f32_16x16x128_f8f6f4 v[52:55], v[160:167], v[176:183], v[52:55]
	v_mfma_f32_16x16x128_f8f6f4 v[48:51], v[168:175], v[176:183], v[48:51]
	v_mfma_f32_16x16x128_f8f6f4 v[36:39], v[160:167], v[184:191], v[36:39]
	v_mfma_f32_16x16x128_f8f6f4 v[32:35], v[168:175], v[184:191], v[32:35]
	v_mfma_f32_16x16x128_f8f6f4 v[20:23], v[160:167], v[196:203], v[20:23]
	v_mfma_f32_16x16x128_f8f6f4 v[16:19], v[168:175], v[196:203], v[16:19]
	v_mfma_f32_16x16x128_f8f6f4 v[4:7], v[160:167], v[204:211], v[4:7]
	v_mfma_f32_16x16x128_f8f6f4 v[0:3], v[168:175], v[204:211], v[0:3]
	s_setprio 0
	s_barrier
	s_mov_b32 m0, s58
	v_lshl_add_u64 v[140:141], s[34:35], 0, v[130:131]
	global_load_lds_dwordx4 v[140:141], off
	v_lshl_add_u64 v[140:141], s[34:35], 0, v[128:129]
	s_mov_b32 m0, s59
	s_andn2_b64 vcc, exec, s[28:29]
	global_load_lds_dwordx4 v[140:141], off
	s_mov_b64 s[30:31], -1
	s_mov_b64 s[28:29], 0
	s_mov_b64 s[34:35], 0x100
	s_cbranch_vccz .LBB0_1081
	s_branch .Lpeel_after_1081

.Lpeel_after_1081:
	s_and_b64 vcc, exec, s[8:9]
	s_cbranch_vccz .LBB0_1084
	s_barrier

.LBB0_1960:
	v_mov_b32_e32 v137, v133
	v_mov_b32_e32 v139, v133
	s_mov_b64 s[44:45], 0
	s_mov_b64 s[40:41], -1
	s_mov_b64 s[42:43], 0
	s_add_u32 s52, s12, s44
	s_addc_u32 s53, s13, s45
	s_add_u32 s29, s52, 0x100
	s_addc_u32 s48, s53, 0
	s_and_b64 s[46:47], s[42:43], exec
	s_cselect_b32 s46, s12, s29
	s_cselect_b32 s47, s13, s48
	s_add_u32 s29, s38, s44
	s_addc_u32 s44, s39, s45
	s_add_u32 s29, s29, 0x100
	s_addc_u32 s48, s44, 0
	ds_read_b128 v[162:165], v147
	ds_read_b128 v[170:173], v147 offset:2048
	ds_read_b128 v[166:169], v148
	ds_read_b128 v[174:177], v148 offset:2048
	s_and_b64 s[44:45], s[42:43], exec
	s_cselect_b32 s51, s35, s48
	s_cselect_b32 s50, s34, s29
	s_add_i32 m0, s0, 0xc000
	s_add_i32 s29, s0, 0xe000
	s_add_u32 s48, s50, 0x1000
	s_addc_u32 s49, s51, 0
	s_add_u32 s44, s50, 0x1080
	s_addc_u32 s45, s51, 0
	v_cndmask_b32_e64 v132, v135, v157, s[42:43]
	v_cndmask_b32_e64 v161, v136, v159, s[42:43]
	v_lshl_add_u64 v[140:141], s[52:53], 0, v[136:137]
	v_lshl_add_u64 v[140:141], v[140:141], 0, s[20:21]
	ds_read_b128 v[178:181], v145
	ds_read_b128 v[186:189], v145 offset:2048
	ds_read_b128 v[182:185], v146
	ds_read_b128 v[190:193], v146 offset:2048
	ds_read_b128 v[196:199], v145 offset:4096
	ds_read_b128 v[204:207], v145 offset:6144
	ds_read_b128 v[200:203], v146 offset:4096
	ds_read_b128 v[208:211], v146 offset:6144
	global_load_lds_dwordx4 v[140:141], off
	v_lshl_add_u64 v[140:141], s[52:53], 0, v[138:139]
	v_lshl_add_u64 v[140:141], v[140:141], 0, s[20:21]
	s_mov_b32 m0, s29
	s_nop 0
	global_load_lds_dwordx4 v[140:141], off
	s_waitcnt lgkmcnt(8)
	s_barrier
	s_waitcnt lgkmcnt(0)
	v_cndmask_b32_e64 v140, v134, v158, s[42:43]
	s_setprio 1
	s_waitcnt lgkmcnt(0)
	v_mfma_f32_16x16x128_f8f6f4 v[124:127], v[162:169], v[178:185], 0
	v_mfma_f32_16x16x128_f8f6f4 v[120:123], v[170:177], v[178:185], 0
	v_mfma_f32_16x16x128_f8f6f4 v[108:111], v[162:169], v[186:193], 0
	v_mfma_f32_16x16x128_f8f6f4 v[104:107], v[170:177], v[186:193], 0
	v_mfma_f32_16x16x128_f8f6f4 v[92:95], v[162:169], v[196:203], 0
	v_mfma_f32_16x16x128_f8f6f4 v[88:91], v[170:177], v[196:203], 0
	v_mfma_f32_16x16x128_f8f6f4 v[76:79], v[162:169], v[204:211], 0
	v_mfma_f32_16x16x128_f8f6f4 v[72:75], v[170:177], v[204:211], 0
	s_setprio 0
	s_barrier
	ds_read_b128 v[162:165], v147 offset:16384
	ds_read_b128 v[170:173], v147 offset:18432
	ds_read_b128 v[166:169], v148 offset:16384
	ds_read_b128 v[174:177], v148 offset:18432
	s_barrier
	s_waitcnt lgkmcnt(0)
	s_setprio 1
	s_waitcnt lgkmcnt(0)
	v_mfma_f32_16x16x128_f8f6f4 v[116:119], v[162:169], v[178:185], 0
	v_mfma_f32_16x16x128_f8f6f4 v[112:115], v[170:177], v[178:185], 0
	v_mfma_f32_16x16x128_f8f6f4 v[100:103], v[162:169], v[186:193], 0
	v_mfma_f32_16x16x128_f8f6f4 v[96:99], v[170:177], v[186:193], 0
	v_mfma_f32_16x16x128_f8f6f4 v[84:87], v[162:169], v[196:203], 0
	v_mfma_f32_16x16x128_f8f6f4 v[80:83], v[170:177], v[196:203], 0
	v_mfma_f32_16x16x128_f8f6f4 v[68:71], v[162:169], v[204:211], 0
	v_mfma_f32_16x16x128_f8f6f4 v[64:67], v[170:177], v[204:211], 0
	s_setprio 0
	s_barrier
	ds_read_b128 v[162:165], v147
	ds_read_b128 v[170:173], v147 offset:2048
	ds_read_b128 v[166:169], v148
	ds_read_b128 v[174:177], v148 offset:2048
	s_mov_b32 m0, s0
	ds_read_b128 v[178:181], v145 offset:16384
	ds_read_b128 v[186:189], v145 offset:18432
	ds_read_b128 v[182:185], v146 offset:16384
	ds_read_b128 v[190:193], v146 offset:18432
	ds_read_b128 v[196:199], v145 offset:20480
	ds_read_b128 v[204:207], v145 offset:22528
	ds_read_b128 v[200:203], v146 offset:20480
	ds_read_b128 v[208:211], v146 offset:22528
	global_load_lds_dwordx4 v132, s[46:47]
	s_mov_b32 m0, s56
	v_mov_b32_e32 v141, v133
	global_load_lds_dwordx4 v140, s[46:47]
	s_waitcnt lgkmcnt(8)
	s_barrier
	s_waitcnt lgkmcnt(0)
	v_lshl_add_u64 v[212:213], s[46:47], 0, v[132:133]
	v_lshl_add_u64 v[214:215], s[46:47], 0, v[140:141]
	s_setprio 1
	s_waitcnt lgkmcnt(0)
	v_mfma_f32_16x16x128_f8f6f4 v[60:63], v[162:169], v[178:185], 0
	v_mfma_f32_16x16x128_f8f6f4 v[56:59], v[170:177], v[178:185], 0
	v_mfma_f32_16x16x128_f8f6f4 v[44:47], v[162:169], v[186:193], 0
	v_mfma_f32_16x16x128_f8f6f4 v[40:43], v[170:177], v[186:193], 0
	v_mfma_f32_16x16x128_f8f6f4 v[28:31], v[162:169], v[196:203], 0
	v_mfma_f32_16x16x128_f8f6f4 v[24:27], v[170:177], v[196:203], 0
	v_mfma_f32_16x16x128_f8f6f4 v[12:15], v[162:169], v[204:211], 0
	v_mfma_f32_16x16x128_f8f6f4 v[8:11], v[170:177], v[204:211], 0
	s_setprio 0
	s_barrier
	s_mov_b32 m0, s1
	v_lshl_add_u64 v[140:141], s[50:51], 0, v[128:129]
	ds_read_b128 v[162:165], v147 offset:16384
	ds_read_b128 v[170:173], v147 offset:18432
	ds_read_b128 v[166:169], v148 offset:16384
	ds_read_b128 v[174:177], v148 offset:18432
	global_load_lds_dwordx4 v[140:141], off
	v_lshl_add_u64 v[142:143], s[50:51], 0, v[130:131]
	s_mov_b32 m0, s37
	s_nop 0
	global_load_lds_dwordx4 v[142:143], off
	s_waitcnt vmcnt(4)
	s_waitcnt lgkmcnt(0)
	s_barrier
	s_setprio 1
	s_waitcnt lgkmcnt(0)
	v_mfma_f32_16x16x128_f8f6f4 v[52:55], v[162:169], v[178:185], 0
	v_mfma_f32_16x16x128_f8f6f4 v[48:51], v[170:177], v[178:185], 0
	v_mfma_f32_16x16x128_f8f6f4 v[36:39], v[162:169], v[186:193], 0
	v_mfma_f32_16x16x128_f8f6f4 v[32:35], v[170:177], v[186:193], 0
	v_mfma_f32_16x16x128_f8f6f4 v[20:23], v[162:169], v[196:203], 0
	v_mfma_f32_16x16x128_f8f6f4 v[16:19], v[170:177], v[196:203], 0
	v_mfma_f32_16x16x128_f8f6f4 v[4:7], v[162:169], v[204:211], 0
	v_mfma_f32_16x16x128_f8f6f4 v[0:3], v[170:177], v[204:211], 0
	s_setprio 0
	s_barrier
	ds_read_b128 v[162:165], v147 offset:32768
	ds_read_b128 v[170:173], v147 offset:34816
	ds_read_b128 v[166:169], v148 offset:32768
	ds_read_b128 v[174:177], v148 offset:34816
	s_mov_b32 m0, s65
	ds_read_b128 v[178:181], v145 offset:32768
	ds_read_b128 v[186:189], v145 offset:34816
	ds_read_b128 v[182:185], v146 offset:32768
	ds_read_b128 v[190:193], v146 offset:34816
	ds_read_b128 v[196:199], v145 offset:36864
	ds_read_b128 v[204:207], v145 offset:38912
	ds_read_b128 v[200:203], v146 offset:36864
	ds_read_b128 v[208:211], v146 offset:38912
	v_cndmask_b32_e64 v132, v138, v160, s[42:43]
	global_load_lds_dwordx4 v161, s[46:47]
	s_mov_b32 m0, s66
	v_lshl_add_u64 v[216:217], s[48:49], 0, v[128:129]
	global_load_lds_dwordx4 v132, s[46:47]
	s_mov_b32 m0, s57
	s_nop 0
	global_load_lds_dwordx4 v[216:217], off
	v_lshl_add_u64 v[216:217], s[48:49], 0, v[130:131]
	s_mov_b32 m0, s64
	s_nop 0
	global_load_lds_dwordx4 v[216:217], off
	s_waitcnt lgkmcnt(8)
	s_barrier
	s_waitcnt lgkmcnt(0)
	s_setprio 1
	s_waitcnt lgkmcnt(0)
	v_mfma_f32_16x16x128_f8f6f4 v[124:127], v[162:169], v[178:185], v[124:127]
	v_mfma_f32_16x16x128_f8f6f4 v[120:123], v[170:177], v[178:185], v[120:123]
	v_mfma_f32_16x16x128_f8f6f4 v[108:111], v[162:169], v[186:193], v[108:111]
	v_mfma_f32_16x16x128_f8f6f4 v[104:107], v[170:177], v[186:193], v[104:107]
	v_mfma_f32_16x16x128_f8f6f4 v[92:95], v[162:169], v[196:203], v[92:95]
	v_mfma_f32_16x16x128_f8f6f4 v[88:91], v[170:177], v[196:203], v[88:91]
	v_mfma_f32_16x16x128_f8f6f4 v[76:79], v[162:169], v[204:211], v[76:79]
	v_mfma_f32_16x16x128_f8f6f4 v[72:75], v[170:177], v[204:211], v[72:75]
	s_setprio 0
	s_barrier
	ds_read_b128 v[162:165], v147 offset:49152
	ds_read_b128 v[170:173], v147 offset:51200
	ds_read_b128 v[166:169], v148 offset:49152
	ds_read_b128 v[174:177], v148 offset:51200
	s_barrier
	s_waitcnt lgkmcnt(0)
	s_setprio 1
	s_waitcnt lgkmcnt(0)
	v_mfma_f32_16x16x128_f8f6f4 v[116:119], v[162:169], v[178:185], v[116:119]
	v_mfma_f32_16x16x128_f8f6f4 v[112:115], v[170:177], v[178:185], v[112:115]
	v_mfma_f32_16x16x128_f8f6f4 v[100:103], v[162:169], v[186:193], v[100:103]
	v_mfma_f32_16x16x128_f8f6f4 v[96:99], v[170:177], v[186:193], v[96:99]
	v_mfma_f32_16x16x128_f8f6f4 v[84:87], v[162:169], v[196:203], v[84:87]
	v_mfma_f32_16x16x128_f8f6f4 v[80:83], v[170:177], v[196:203], v[80:83]
	v_mfma_f32_16x16x128_f8f6f4 v[68:71], v[162:169], v[204:211], v[68:71]
	v_mfma_f32_16x16x128_f8f6f4 v[64:67], v[170:177], v[204:211], v[64:67]
	s_setprio 0
	s_barrier
	ds_read_b128 v[162:165], v147 offset:32768
	ds_read_b128 v[170:173], v147 offset:34816
	ds_read_b128 v[166:169], v148 offset:32768
	ds_read_b128 v[174:177], v148 offset:34816
	s_mov_b32 m0, s69
	v_lshl_add_u64 v[212:213], v[212:213], 0, s[20:21]
	ds_read_b128 v[178:181], v145 offset:49152
	ds_read_b128 v[186:189], v145 offset:51200
	ds_read_b128 v[182:185], v146 offset:49152
	ds_read_b128 v[190:193], v146 offset:51200
	ds_read_b128 v[196:199], v145 offset:53248
	ds_read_b128 v[204:207], v145 offset:55296
	ds_read_b128 v[200:203], v146 offset:53248
	ds_read_b128 v[208:211], v146 offset:55296
	global_load_lds_dwordx4 v[212:213], off
	v_lshl_add_u64 v[212:213], v[214:215], 0, s[20:21]
	s_mov_b32 m0, s70
	s_nop 0
	global_load_lds_dwordx4 v[212:213], off
	s_waitcnt lgkmcnt(8)
	s_barrier
	s_waitcnt lgkmcnt(0)
	s_setprio 1
	s_waitcnt lgkmcnt(0)
	v_mfma_f32_16x16x128_f8f6f4 v[60:63], v[162:169], v[178:185], v[60:63]
	v_mfma_f32_16x16x128_f8f6f4 v[56:59], v[170:177], v[178:185], v[56:59]
	v_mfma_f32_16x16x128_f8f6f4 v[44:47], v[162:169], v[186:193], v[44:47]
	v_mfma_f32_16x16x128_f8f6f4 v[40:43], v[170:177], v[186:193], v[40:43]
	v_mfma_f32_16x16x128_f8f6f4 v[28:31], v[162:169], v[196:203], v[28:31]
	v_mfma_f32_16x16x128_f8f6f4 v[24:27], v[170:177], v[196:203], v[24:27]
	v_mfma_f32_16x16x128_f8f6f4 v[12:15], v[162:169], v[204:211], v[12:15]
	v_mfma_f32_16x16x128_f8f6f4 v[8:11], v[170:177], v[204:211], v[8:11]
	s_setprio 0
	s_barrier
	s_mov_b32 m0, s67
	v_lshl_add_u64 v[140:141], v[140:141], 0, s[20:21]
	ds_read_b128 v[162:165], v147 offset:49152
	ds_read_b128 v[170:173], v147 offset:51200
	ds_read_b128 v[166:169], v148 offset:49152
	ds_read_b128 v[174:177], v148 offset:51200
	global_load_lds_dwordx4 v[140:141], off
	v_lshl_add_u64 v[140:141], v[142:143], 0, s[20:21]
	s_mov_b32 m0, s68
	s_nop 0
	global_load_lds_dwordx4 v[140:141], off
	s_waitcnt vmcnt(4)
	s_waitcnt lgkmcnt(0)
	s_barrier
	s_setprio 1
	s_waitcnt lgkmcnt(0)
	v_mfma_f32_16x16x128_f8f6f4 v[52:55], v[162:169], v[178:185], v[52:55]
	v_mfma_f32_16x16x128_f8f6f4 v[48:51], v[170:177], v[178:185], v[48:51]
	v_mfma_f32_16x16x128_f8f6f4 v[36:39], v[162:169], v[186:193], v[36:39]
	v_mfma_f32_16x16x128_f8f6f4 v[32:35], v[170:177], v[186:193], v[32:35]
	v_mfma_f32_16x16x128_f8f6f4 v[20:23], v[162:169], v[196:203], v[20:23]
	v_mfma_f32_16x16x128_f8f6f4 v[16:19], v[170:177], v[196:203], v[16:19]
	v_mfma_f32_16x16x128_f8f6f4 v[4:7], v[162:169], v[204:211], v[4:7]
	v_mfma_f32_16x16x128_f8f6f4 v[0:3], v[170:177], v[204:211], v[0:3]
	s_setprio 0
	s_barrier
	s_mov_b32 m0, s71
	v_lshl_add_u64 v[140:141], s[44:45], 0, v[128:129]
	global_load_lds_dwordx4 v[140:141], off
	v_lshl_add_u64 v[140:141], s[44:45], 0, v[130:131]
	s_mov_b32 m0, s72
	s_andn2_b64 vcc, exec, s[40:41]
	global_load_lds_dwordx4 v[140:141], off
	s_mov_b64 s[42:43], -1
	s_mov_b64 s[40:41], 0
	s_mov_b64 s[44:45], 0x100
	s_cbranch_vccz .LBB0_1961
	s_branch .Lpeel_after_1961

.LBB0_1988:
	v_mov_b32_e32 v137, v133
	v_mov_b32_e32 v139, v133
	s_mov_b64 s[34:35], 0
	s_mov_b64 s[28:29], -1
	s_mov_b64 s[30:31], 0
	s_add_u32 s42, s10, s34
	s_addc_u32 s43, s11, s35
	s_add_u32 s38, s42, 0x100
	s_addc_u32 s39, s43, 0
	s_and_b64 s[36:37], s[30:31], exec
	s_cselect_b32 s36, s10, s38
	s_cselect_b32 s37, s11, s39
	s_add_u32 s34, s26, s34
	s_addc_u32 s35, s27, s35
	s_add_u32 s38, s34, 0x100
	s_addc_u32 s39, s35, 0
	ds_read_b128 v[160:163], v147
	ds_read_b128 v[168:171], v147 offset:2048
	ds_read_b128 v[164:167], v148
	ds_read_b128 v[172:175], v148 offset:2048
	s_and_b64 s[34:35], s[30:31], exec
	s_cselect_b32 s41, s25, s39
	s_cselect_b32 s40, s24, s38
	s_add_i32 m0, s0, 0xc000
	s_add_i32 s62, s0, 0xe000
	s_add_u32 s38, s40, 0x1000
	s_addc_u32 s39, s41, 0
	s_add_u32 s34, s40, 0x1080
	s_addc_u32 s35, s41, 0
	v_cndmask_b32_e64 v132, v135, v155, s[30:31]
	v_cndmask_b32_e64 v159, v136, v157, s[30:31]
	v_lshl_add_u64 v[140:141], s[42:43], 0, v[136:137]
	v_lshl_add_u64 v[140:141], v[140:141], 0, s[16:17]
	ds_read_b128 v[176:179], v145
	ds_read_b128 v[184:187], v145 offset:2048
	ds_read_b128 v[180:183], v146
	ds_read_b128 v[188:191], v146 offset:2048
	ds_read_b128 v[196:199], v145 offset:4096
	ds_read_b128 v[204:207], v145 offset:6144
	ds_read_b128 v[200:203], v146 offset:4096
	ds_read_b128 v[208:211], v146 offset:6144
	global_load_lds_dwordx4 v[140:141], off
	v_lshl_add_u64 v[140:141], s[42:43], 0, v[138:139]
	v_lshl_add_u64 v[140:141], v[140:141], 0, s[16:17]
	s_mov_b32 m0, s62
	s_nop 0
	global_load_lds_dwordx4 v[140:141], off
	s_waitcnt lgkmcnt(8)
	s_barrier
	s_waitcnt lgkmcnt(0)
	v_cndmask_b32_e64 v140, v134, v156, s[30:31]
	s_setprio 1
	s_waitcnt lgkmcnt(0)
	v_mfma_f32_16x16x128_f8f6f4 v[124:127], v[160:167], v[176:183], 0
	v_mfma_f32_16x16x128_f8f6f4 v[120:123], v[168:175], v[176:183], 0
	v_mfma_f32_16x16x128_f8f6f4 v[108:111], v[160:167], v[184:191], 0
	v_mfma_f32_16x16x128_f8f6f4 v[104:107], v[168:175], v[184:191], 0
	v_mfma_f32_16x16x128_f8f6f4 v[92:95], v[160:167], v[196:203], 0
	v_mfma_f32_16x16x128_f8f6f4 v[88:91], v[168:175], v[196:203], 0
	v_mfma_f32_16x16x128_f8f6f4 v[76:79], v[160:167], v[204:211], 0
	v_mfma_f32_16x16x128_f8f6f4 v[72:75], v[168:175], v[204:211], 0
	s_setprio 0
	s_barrier
	ds_read_b128 v[160:163], v147 offset:16384
	ds_read_b128 v[168:171], v147 offset:18432
	ds_read_b128 v[164:167], v148 offset:16384
	ds_read_b128 v[172:175], v148 offset:18432
	s_barrier
	s_waitcnt lgkmcnt(0)
	s_setprio 1
	s_waitcnt lgkmcnt(0)
	v_mfma_f32_16x16x128_f8f6f4 v[116:119], v[160:167], v[176:183], 0
	v_mfma_f32_16x16x128_f8f6f4 v[112:115], v[168:175], v[176:183], 0
	v_mfma_f32_16x16x128_f8f6f4 v[100:103], v[160:167], v[184:191], 0
	v_mfma_f32_16x16x128_f8f6f4 v[96:99], v[168:175], v[184:191], 0
	v_mfma_f32_16x16x128_f8f6f4 v[84:87], v[160:167], v[196:203], 0
	v_mfma_f32_16x16x128_f8f6f4 v[80:83], v[168:175], v[196:203], 0
	v_mfma_f32_16x16x128_f8f6f4 v[68:71], v[160:167], v[204:211], 0
	v_mfma_f32_16x16x128_f8f6f4 v[64:67], v[168:175], v[204:211], 0
	s_setprio 0
	s_barrier
	ds_read_b128 v[160:163], v147
	ds_read_b128 v[168:171], v147 offset:2048
	ds_read_b128 v[164:167], v148
	ds_read_b128 v[172:175], v148 offset:2048
	s_mov_b32 m0, s0
	ds_read_b128 v[176:179], v145 offset:16384
	ds_read_b128 v[184:187], v145 offset:18432
	ds_read_b128 v[180:183], v146 offset:16384
	ds_read_b128 v[188:191], v146 offset:18432
	ds_read_b128 v[196:199], v145 offset:20480
	ds_read_b128 v[204:207], v145 offset:22528
	ds_read_b128 v[200:203], v146 offset:20480
	ds_read_b128 v[208:211], v146 offset:22528
	global_load_lds_dwordx4 v132, s[36:37]
	s_mov_b32 m0, s47
	v_mov_b32_e32 v141, v133
	global_load_lds_dwordx4 v140, s[36:37]
	s_waitcnt lgkmcnt(8)
	s_barrier
	s_waitcnt lgkmcnt(0)
	v_lshl_add_u64 v[192:193], s[36:37], 0, v[132:133]
	v_lshl_add_u64 v[212:213], s[36:37], 0, v[140:141]
	s_setprio 1
	s_waitcnt lgkmcnt(0)
	v_mfma_f32_16x16x128_f8f6f4 v[60:63], v[160:167], v[176:183], 0
	v_mfma_f32_16x16x128_f8f6f4 v[56:59], v[168:175], v[176:183], 0
	v_mfma_f32_16x16x128_f8f6f4 v[44:47], v[160:167], v[184:191], 0
	v_mfma_f32_16x16x128_f8f6f4 v[40:43], v[168:175], v[184:191], 0
	v_mfma_f32_16x16x128_f8f6f4 v[28:31], v[160:167], v[196:203], 0
	v_mfma_f32_16x16x128_f8f6f4 v[24:27], v[168:175], v[196:203], 0
	v_mfma_f32_16x16x128_f8f6f4 v[12:15], v[160:167], v[204:211], 0
	v_mfma_f32_16x16x128_f8f6f4 v[8:11], v[168:175], v[204:211], 0
	s_setprio 0
	s_barrier
	s_mov_b32 m0, s1
	v_lshl_add_u64 v[140:141], s[40:41], 0, v[128:129]
	ds_read_b128 v[160:163], v147 offset:16384
	ds_read_b128 v[168:171], v147 offset:18432
	ds_read_b128 v[164:167], v148 offset:16384
	ds_read_b128 v[172:175], v148 offset:18432
	global_load_lds_dwordx4 v[140:141], off
	v_lshl_add_u64 v[142:143], s[40:41], 0, v[130:131]
	s_mov_b32 m0, s46
	s_nop 0
	global_load_lds_dwordx4 v[142:143], off
	s_waitcnt vmcnt(4)
	s_waitcnt lgkmcnt(0)
	s_barrier
	s_setprio 1
	s_waitcnt lgkmcnt(0)
	v_mfma_f32_16x16x128_f8f6f4 v[52:55], v[160:167], v[176:183], 0
	v_mfma_f32_16x16x128_f8f6f4 v[48:51], v[168:175], v[176:183], 0
	v_mfma_f32_16x16x128_f8f6f4 v[36:39], v[160:167], v[184:191], 0
	v_mfma_f32_16x16x128_f8f6f4 v[32:35], v[168:175], v[184:191], 0
	v_mfma_f32_16x16x128_f8f6f4 v[20:23], v[160:167], v[196:203], 0
	v_mfma_f32_16x16x128_f8f6f4 v[16:19], v[168:175], v[196:203], 0
	v_mfma_f32_16x16x128_f8f6f4 v[4:7], v[160:167], v[204:211], 0
	v_mfma_f32_16x16x128_f8f6f4 v[0:3], v[168:175], v[204:211], 0
	s_setprio 0
	s_barrier
	ds_read_b128 v[160:163], v147 offset:32768
	ds_read_b128 v[168:171], v147 offset:34816
	ds_read_b128 v[164:167], v148 offset:32768
	ds_read_b128 v[172:175], v148 offset:34816
	s_mov_b32 m0, s50
	ds_read_b128 v[176:179], v145 offset:32768
	ds_read_b128 v[184:187], v145 offset:34816
	ds_read_b128 v[180:183], v146 offset:32768
	ds_read_b128 v[188:191], v146 offset:34816
	ds_read_b128 v[196:199], v145 offset:36864
	ds_read_b128 v[204:207], v145 offset:38912
	ds_read_b128 v[200:203], v146 offset:36864
	ds_read_b128 v[208:211], v146 offset:38912
	v_cndmask_b32_e64 v132, v138, v158, s[30:31]
	global_load_lds_dwordx4 v159, s[36:37]
	s_mov_b32 m0, s51
	v_lshl_add_u64 v[214:215], s[38:39], 0, v[128:129]
	global_load_lds_dwordx4 v132, s[36:37]
	s_mov_b32 m0, s48
	s_nop 0
	global_load_lds_dwordx4 v[214:215], off
	v_lshl_add_u64 v[214:215], s[38:39], 0, v[130:131]
	s_mov_b32 m0, s49
	s_nop 0
	global_load_lds_dwordx4 v[214:215], off
	s_waitcnt lgkmcnt(8)
	s_barrier
	s_waitcnt lgkmcnt(0)
	s_setprio 1
	s_waitcnt lgkmcnt(0)
	v_mfma_f32_16x16x128_f8f6f4 v[124:127], v[160:167], v[176:183], v[124:127]
	v_mfma_f32_16x16x128_f8f6f4 v[120:123], v[168:175], v[176:183], v[120:123]
	v_mfma_f32_16x16x128_f8f6f4 v[108:111], v[160:167], v[184:191], v[108:111]
	v_mfma_f32_16x16x128_f8f6f4 v[104:107], v[168:175], v[184:191], v[104:107]
	v_mfma_f32_16x16x128_f8f6f4 v[92:95], v[160:167], v[196:203], v[92:95]
	v_mfma_f32_16x16x128_f8f6f4 v[88:91], v[168:175], v[196:203], v[88:91]
	v_mfma_f32_16x16x128_f8f6f4 v[76:79], v[160:167], v[204:211], v[76:79]
	v_mfma_f32_16x16x128_f8f6f4 v[72:75], v[168:175], v[204:211], v[72:75]
	s_setprio 0
	s_barrier
	ds_read_b128 v[160:163], v147 offset:49152
	ds_read_b128 v[168:171], v147 offset:51200
	ds_read_b128 v[164:167], v148 offset:49152
	ds_read_b128 v[172:175], v148 offset:51200
	s_barrier
	s_waitcnt lgkmcnt(0)
	s_setprio 1
	s_waitcnt lgkmcnt(0)
	v_mfma_f32_16x16x128_f8f6f4 v[116:119], v[160:167], v[176:183], v[116:119]
	v_mfma_f32_16x16x128_f8f6f4 v[112:115], v[168:175], v[176:183], v[112:115]
	v_mfma_f32_16x16x128_f8f6f4 v[100:103], v[160:167], v[184:191], v[100:103]
	v_mfma_f32_16x16x128_f8f6f4 v[96:99], v[168:175], v[184:191], v[96:99]
	v_mfma_f32_16x16x128_f8f6f4 v[84:87], v[160:167], v[196:203], v[84:87]
	v_mfma_f32_16x16x128_f8f6f4 v[80:83], v[168:175], v[196:203], v[80:83]
	v_mfma_f32_16x16x128_f8f6f4 v[68:71], v[160:167], v[204:211], v[68:71]
	v_mfma_f32_16x16x128_f8f6f4 v[64:67], v[168:175], v[204:211], v[64:67]
	s_setprio 0
	s_barrier
	ds_read_b128 v[160:163], v147 offset:32768
	ds_read_b128 v[168:171], v147 offset:34816
	ds_read_b128 v[164:167], v148 offset:32768
	ds_read_b128 v[172:175], v148 offset:34816
	s_mov_b32 m0, s55
	v_lshl_add_u64 v[192:193], v[192:193], 0, s[16:17]
	ds_read_b128 v[176:179], v145 offset:49152
	ds_read_b128 v[184:187], v145 offset:51200
	ds_read_b128 v[180:183], v146 offset:49152
	ds_read_b128 v[188:191], v146 offset:51200
	ds_read_b128 v[196:199], v145 offset:53248
	ds_read_b128 v[204:207], v145 offset:55296
	ds_read_b128 v[200:203], v146 offset:53248
	ds_read_b128 v[208:211], v146 offset:55296
	global_load_lds_dwordx4 v[192:193], off
	v_lshl_add_u64 v[192:193], v[212:213], 0, s[16:17]
	s_mov_b32 m0, s56
	s_nop 0
	global_load_lds_dwordx4 v[192:193], off
	s_waitcnt lgkmcnt(8)
	s_barrier
	s_waitcnt lgkmcnt(0)
	s_setprio 1
	s_waitcnt lgkmcnt(0)
	v_mfma_f32_16x16x128_f8f6f4 v[60:63], v[160:167], v[176:183], v[60:63]
	v_mfma_f32_16x16x128_f8f6f4 v[56:59], v[168:175], v[176:183], v[56:59]
	v_mfma_f32_16x16x128_f8f6f4 v[44:47], v[160:167], v[184:191], v[44:47]
	v_mfma_f32_16x16x128_f8f6f4 v[40:43], v[168:175], v[184:191], v[40:43]
	v_mfma_f32_16x16x128_f8f6f4 v[28:31], v[160:167], v[196:203], v[28:31]
	v_mfma_f32_16x16x128_f8f6f4 v[24:27], v[168:175], v[196:203], v[24:27]
	v_mfma_f32_16x16x128_f8f6f4 v[12:15], v[160:167], v[204:211], v[12:15]
	v_mfma_f32_16x16x128_f8f6f4 v[8:11], v[168:175], v[204:211], v[8:11]
	s_setprio 0
	s_barrier
	s_mov_b32 m0, s53
	v_lshl_add_u64 v[140:141], v[140:141], 0, s[16:17]
	ds_read_b128 v[160:163], v147 offset:49152
	ds_read_b128 v[168:171], v147 offset:51200
	ds_read_b128 v[164:167], v148 offset:49152
	ds_read_b128 v[172:175], v148 offset:51200
	global_load_lds_dwordx4 v[140:141], off
	v_lshl_add_u64 v[140:141], v[142:143], 0, s[16:17]
	s_mov_b32 m0, s54
	s_nop 0
	global_load_lds_dwordx4 v[140:141], off
	s_waitcnt vmcnt(4)
	s_waitcnt lgkmcnt(0)
	s_barrier
	s_setprio 1
	s_waitcnt lgkmcnt(0)
	v_mfma_f32_16x16x128_f8f6f4 v[52:55], v[160:167], v[176:183], v[52:55]
	v_mfma_f32_16x16x128_f8f6f4 v[48:51], v[168:175], v[176:183], v[48:51]
	v_mfma_f32_16x16x128_f8f6f4 v[36:39], v[160:167], v[184:191], v[36:39]
	v_mfma_f32_16x16x128_f8f6f4 v[32:35], v[168:175], v[184:191], v[32:35]
	v_mfma_f32_16x16x128_f8f6f4 v[20:23], v[160:167], v[196:203], v[20:23]
	v_mfma_f32_16x16x128_f8f6f4 v[16:19], v[168:175], v[196:203], v[16:19]
	v_mfma_f32_16x16x128_f8f6f4 v[4:7], v[160:167], v[204:211], v[4:7]
	v_mfma_f32_16x16x128_f8f6f4 v[0:3], v[168:175], v[204:211], v[0:3]
	s_setprio 0
	s_barrier
	s_mov_b32 m0, s57
	v_lshl_add_u64 v[140:141], s[34:35], 0, v[128:129]
	global_load_lds_dwordx4 v[140:141], off
	v_lshl_add_u64 v[140:141], s[34:35], 0, v[130:131]
	s_mov_b32 m0, s58
	s_andn2_b64 vcc, exec, s[28:29]
	global_load_lds_dwordx4 v[140:141], off
	s_mov_b64 s[30:31], -1
	s_mov_b64 s[28:29], 0
	s_mov_b64 s[34:35], 0x100
	s_cbranch_vccz .LBB0_1989
	s_branch .Lpeel_after_1989
